# K-loops: redundant lgkmcnt(0) after the pre-MFMA barrier and the mid-segment setprio 0/1 pair removed
# speedup vs baseline: 1.0144x; 1.0144x over previous
.LBB0_235:
	s_add_u32 s4, s0, 0xfffe0080
	s_addc_u32 s5, s1, -1
	s_add_i32 s52, 0, 0x10000
	s_cmp_eq_u32 s51, 4
	s_cselect_b32 s7, s21, s5
	s_cselect_b32 s6, s29, s4
	s_cselect_b32 s5, s23, s50
	s_cselect_b32 s4, s48, s49
	s_add_i32 s53, 0, 0x14000
	ds_read_b128 v[20:23], v192
	ds_read_b128 v[24:27], v249
	ds_read_b128 v[28:31], v192 offset:2048
	ds_read_b128 v[32:35], v249 offset:2048
	ds_read_b128 v[4:7], v192 offset:16384
	ds_read_b128 v[8:11], v249 offset:16384
	ds_read_b128 v[12:15], v192 offset:18432
	ds_read_b128 v[16:19], v249 offset:18432
	v_lshl_add_u64 v[234:235], s[0:1], 0, v[180:181]
	s_add_i32 m0, s37, 0xc000
	ds_read_b128 v[184:187], v193
	ds_read_b128 v[188:191], v250
	ds_read_b128 v[194:197], v193 offset:2048
	ds_read_b128 v[198:201], v250 offset:2048
	ds_read_b128 v[202:205], v193 offset:4096
	ds_read_b128 v[206:209], v250 offset:4096
	ds_read_b128 v[226:229], v193 offset:6144
	ds_read_b128 v[230:233], v250 offset:6144
	global_load_lds_dwordx4 v[234:235], off
	v_lshl_add_u64 v[234:235], s[0:1], 0, v[182:183]
	s_add_i32 m0, s37, 0xe000
	s_nop 0
	global_load_lds_dwordx4 v[234:235], off
	s_waitcnt vmcnt(8)
	s_waitcnt lgkmcnt(0)
	s_barrier
	s_setprio 1
	v_mfma_f32_16x16x128_f8f6f4 v[96:99], v[20:27], v[184:191], v[96:99]
	v_mfma_f32_16x16x128_f8f6f4 v[92:95], v[28:35], v[184:191], v[92:95]
	v_mfma_f32_16x16x128_f8f6f4 v[88:91], v[20:27], v[194:201], v[88:91]
	v_mfma_f32_16x16x128_f8f6f4 v[84:87], v[28:35], v[194:201], v[84:87]
	v_mfma_f32_16x16x128_f8f6f4 v[80:83], v[20:27], v[202:209], v[80:83]
	v_mfma_f32_16x16x128_f8f6f4 v[76:79], v[28:35], v[202:209], v[76:79]
	v_mfma_f32_16x16x128_f8f6f4 v[72:75], v[20:27], v[226:233], v[72:75]
	v_mfma_f32_16x16x128_f8f6f4 v[68:71], v[28:35], v[226:233], v[68:71]
	v_mfma_f32_16x16x128_f8f6f4 v[160:163], v[4:11], v[184:191], v[160:163]
	v_mfma_f32_16x16x128_f8f6f4 v[156:159], v[12:19], v[184:191], v[156:159]
	v_mfma_f32_16x16x128_f8f6f4 v[152:155], v[4:11], v[194:201], v[152:155]
	v_mfma_f32_16x16x128_f8f6f4 v[148:151], v[12:19], v[194:201], v[148:151]
	v_mfma_f32_16x16x128_f8f6f4 v[144:147], v[4:11], v[202:209], v[144:147]
	v_mfma_f32_16x16x128_f8f6f4 v[140:143], v[12:19], v[202:209], v[140:143]
	v_mfma_f32_16x16x128_f8f6f4 v[136:139], v[4:11], v[226:233], v[136:139]
	v_mfma_f32_16x16x128_f8f6f4 v[132:135], v[12:19], v[226:233], v[132:135]
	s_setprio 0
	s_barrier
	s_add_i32 s52, s52, s36
	v_lshl_add_u64 v[184:185], s[4:5], 0, v[176:177]
	s_mov_b32 m0, s52
	ds_read_b128 v[194:197], v193 offset:16384
	ds_read_b128 v[198:201], v250 offset:16384
	ds_read_b128 v[202:205], v193 offset:18432
	ds_read_b128 v[206:209], v250 offset:18432
	ds_read_b128 v[226:229], v193 offset:20480
	ds_read_b128 v[230:233], v250 offset:20480
	ds_read_b128 v[234:237], v193 offset:22528
	ds_read_b128 v[238:241], v250 offset:22528
	global_load_lds_dwordx4 v[184:185], off
	s_add_i32 m0, s52, 0x2000
	s_add_u32 s54, s4, 0x20000
	v_lshl_add_u64 v[186:187], s[4:5], 0, v[172:173]
	s_addc_u32 s55, s5, 0
	s_add_i32 s52, s53, s36
	global_load_lds_dwordx4 v[186:187], off
	v_lshl_add_u64 v[188:189], s[54:55], 0, v[176:177]
	s_mov_b32 m0, s52
	v_lshl_add_u64 v[190:191], s[6:7], 0, v[174:175]
	global_load_lds_dwordx4 v[188:189], off
	v_lshl_add_u64 v[188:189], s[54:55], 0, v[172:173]
	s_add_i32 m0, s52, 0x2000
	s_nop 0
	global_load_lds_dwordx4 v[188:189], off
	v_lshl_add_u64 v[188:189], s[6:7], 0, v[178:179]
	s_mov_b32 m0, s37
	s_nop 0
	global_load_lds_dwordx4 v[188:189], off
	s_mov_b32 m0, s38
	s_nop 0
	global_load_lds_dwordx4 v[190:191], off
	s_waitcnt vmcnt(8)
	s_waitcnt lgkmcnt(0)
	s_barrier
	s_setprio 1
	v_mfma_f32_16x16x128_f8f6f4 v[64:67], v[20:27], v[194:201], v[64:67]
	v_mfma_f32_16x16x128_f8f6f4 v[60:63], v[28:35], v[194:201], v[60:63]
	v_mfma_f32_16x16x128_f8f6f4 v[56:59], v[20:27], v[202:209], v[56:59]
	v_mfma_f32_16x16x128_f8f6f4 v[52:55], v[28:35], v[202:209], v[52:55]
	v_mfma_f32_16x16x128_f8f6f4 v[48:51], v[20:27], v[226:233], v[48:51]
	v_mfma_f32_16x16x128_f8f6f4 v[44:47], v[28:35], v[226:233], v[44:47]
	v_mfma_f32_16x16x128_f8f6f4 v[40:43], v[20:27], v[234:241], v[40:43]
	v_mfma_f32_16x16x128_f8f6f4 v[36:39], v[28:35], v[234:241], v[36:39]
	v_mfma_f32_16x16x128_f8f6f4 v[128:131], v[4:11], v[194:201], v[128:131]
	v_mfma_f32_16x16x128_f8f6f4 v[124:127], v[12:19], v[194:201], v[124:127]
	v_mfma_f32_16x16x128_f8f6f4 v[120:123], v[4:11], v[202:209], v[120:123]
	v_mfma_f32_16x16x128_f8f6f4 v[116:119], v[12:19], v[202:209], v[116:119]
	v_mfma_f32_16x16x128_f8f6f4 v[112:115], v[4:11], v[226:233], v[112:115]
	v_mfma_f32_16x16x128_f8f6f4 v[108:111], v[12:19], v[226:233], v[108:111]
	v_mfma_f32_16x16x128_f8f6f4 v[104:107], v[4:11], v[234:241], v[104:107]
	v_mfma_f32_16x16x128_f8f6f4 v[100:103], v[12:19], v[234:241], v[100:103]
	s_setprio 0
	s_barrier
	s_add_i32 s52, 0, 0x18000
	s_add_i32 s53, 0, 0x1c000
	ds_read_b128 v[4:7], v192 offset:32768
	ds_read_b128 v[8:11], v249 offset:32768
	ds_read_b128 v[12:15], v192 offset:34816
	ds_read_b128 v[16:19], v249 offset:34816
	ds_read_b128 v[20:23], v192 offset:49152
	ds_read_b128 v[24:27], v249 offset:49152
	ds_read_b128 v[28:31], v192 offset:51200
	ds_read_b128 v[32:35], v249 offset:51200
	s_add_u32 s6, s6, 0x20000
	s_addc_u32 s7, s7, 0
	s_mov_b32 m0, s39
	v_lshl_add_u64 v[242:243], s[6:7], 0, v[178:179]
	ds_read_b128 v[194:197], v193 offset:32768
	ds_read_b128 v[198:201], v250 offset:32768
	ds_read_b128 v[202:205], v193 offset:34816
	ds_read_b128 v[206:209], v250 offset:34816
	ds_read_b128 v[226:229], v193 offset:36864
	ds_read_b128 v[230:233], v250 offset:36864
	ds_read_b128 v[234:237], v193 offset:38912
	ds_read_b128 v[238:241], v250 offset:38912
	global_load_lds_dwordx4 v[242:243], off
	v_lshl_add_u64 v[242:243], s[6:7], 0, v[174:175]
	s_mov_b32 m0, s42
	s_nop 0
	global_load_lds_dwordx4 v[242:243], off
	s_waitcnt vmcnt(8)
	s_waitcnt lgkmcnt(0)
	s_barrier
	s_setprio 1
	v_mfma_f32_16x16x128_f8f6f4 v[96:99], v[4:11], v[194:201], v[96:99]
	v_mfma_f32_16x16x128_f8f6f4 v[92:95], v[12:19], v[194:201], v[92:95]
	v_mfma_f32_16x16x128_f8f6f4 v[88:91], v[4:11], v[202:209], v[88:91]
	v_mfma_f32_16x16x128_f8f6f4 v[84:87], v[12:19], v[202:209], v[84:87]
	v_mfma_f32_16x16x128_f8f6f4 v[80:83], v[4:11], v[226:233], v[80:83]
	v_mfma_f32_16x16x128_f8f6f4 v[76:79], v[12:19], v[226:233], v[76:79]
	v_mfma_f32_16x16x128_f8f6f4 v[72:75], v[4:11], v[234:241], v[72:75]
	v_mfma_f32_16x16x128_f8f6f4 v[68:71], v[12:19], v[234:241], v[68:71]
	v_mfma_f32_16x16x128_f8f6f4 v[160:163], v[20:27], v[194:201], v[160:163]
	v_mfma_f32_16x16x128_f8f6f4 v[156:159], v[28:35], v[194:201], v[156:159]
	v_mfma_f32_16x16x128_f8f6f4 v[152:155], v[20:27], v[202:209], v[152:155]
	v_mfma_f32_16x16x128_f8f6f4 v[148:151], v[28:35], v[202:209], v[148:151]
	v_mfma_f32_16x16x128_f8f6f4 v[144:147], v[20:27], v[226:233], v[144:147]
	v_mfma_f32_16x16x128_f8f6f4 v[140:143], v[28:35], v[226:233], v[140:143]
	v_mfma_f32_16x16x128_f8f6f4 v[136:139], v[20:27], v[234:241], v[136:139]
	v_mfma_f32_16x16x128_f8f6f4 v[132:135], v[28:35], v[234:241], v[132:135]
	s_setprio 0
	s_barrier
	s_add_i32 s6, s52, s36
	v_lshl_add_u64 v[184:185], v[184:185], 0, s[56:57]
	s_mov_b32 m0, s6
	ds_read_b128 v[194:197], v193 offset:49152
	ds_read_b128 v[198:201], v250 offset:49152
	ds_read_b128 v[202:205], v193 offset:51200
	ds_read_b128 v[206:209], v250 offset:51200
	ds_read_b128 v[226:229], v193 offset:53248
	ds_read_b128 v[230:233], v250 offset:53248
	ds_read_b128 v[234:237], v193 offset:55296
	ds_read_b128 v[238:241], v250 offset:55296
	global_load_lds_dwordx4 v[184:185], off
	s_add_i32 m0, s6, 0x2000
	s_add_u32 s4, s4, 0x20080
	v_lshl_add_u64 v[184:185], v[186:187], 0, s[56:57]
	s_addc_u32 s5, s5, 0
	s_add_i32 s6, s53, s36
	global_load_lds_dwordx4 v[184:185], off
	v_lshl_add_u64 v[184:185], s[4:5], 0, v[176:177]
	s_mov_b32 m0, s6
	s_nop 0
	global_load_lds_dwordx4 v[184:185], off
	v_lshl_add_u64 v[184:185], s[4:5], 0, v[172:173]
	s_add_i32 m0, s6, 0x2000
	s_nop 0
	global_load_lds_dwordx4 v[184:185], off
	v_lshl_add_u64 v[184:185], v[188:189], 0, s[56:57]
	s_mov_b32 m0, s45
	s_nop 0
	global_load_lds_dwordx4 v[184:185], off
	v_lshl_add_u64 v[184:185], v[190:191], 0, s[56:57]
	s_mov_b32 m0, s46
	s_nop 0
	global_load_lds_dwordx4 v[184:185], off
	s_waitcnt vmcnt(8)
	s_waitcnt lgkmcnt(0)
	s_barrier
	s_setprio 1
	v_mfma_f32_16x16x128_f8f6f4 v[64:67], v[4:11], v[194:201], v[64:67]
	v_mfma_f32_16x16x128_f8f6f4 v[60:63], v[12:19], v[194:201], v[60:63]
	v_mfma_f32_16x16x128_f8f6f4 v[56:59], v[4:11], v[202:209], v[56:59]
	v_mfma_f32_16x16x128_f8f6f4 v[52:55], v[12:19], v[202:209], v[52:55]
	v_mfma_f32_16x16x128_f8f6f4 v[48:51], v[4:11], v[226:233], v[48:51]
	v_mfma_f32_16x16x128_f8f6f4 v[44:47], v[12:19], v[226:233], v[44:47]
	v_mfma_f32_16x16x128_f8f6f4 v[40:43], v[4:11], v[234:241], v[40:43]
	v_mfma_f32_16x16x128_f8f6f4 v[36:39], v[12:19], v[234:241], v[36:39]
	v_mfma_f32_16x16x128_f8f6f4 v[128:131], v[20:27], v[194:201], v[128:131]
	v_mfma_f32_16x16x128_f8f6f4 v[124:127], v[28:35], v[194:201], v[124:127]
	v_mfma_f32_16x16x128_f8f6f4 v[120:123], v[20:27], v[202:209], v[120:123]
	v_mfma_f32_16x16x128_f8f6f4 v[116:119], v[28:35], v[202:209], v[116:119]
	v_mfma_f32_16x16x128_f8f6f4 v[112:115], v[20:27], v[226:233], v[112:115]
	v_mfma_f32_16x16x128_f8f6f4 v[108:111], v[28:35], v[226:233], v[108:111]
	v_mfma_f32_16x16x128_f8f6f4 v[104:107], v[20:27], v[234:241], v[104:107]
	v_mfma_f32_16x16x128_f8f6f4 v[100:103], v[28:35], v[234:241], v[100:103]
	s_setprio 0
	s_barrier
	s_add_i32 s51, s51, 2
	s_add_u32 s0, s0, 0x100
	s_addc_u32 s1, s1, 0
	s_add_u32 s49, s49, 0x100
	s_addc_u32 s50, s50, 0
	s_cmp_gt_u32 s51, 5
	s_cbranch_scc0 .LBB0_235
	s_and_b64 vcc, exec, s[18:19]
	s_cbranch_vccz .LBB0_238
	s_barrier

.LBB0_623:
	s_add_i32 s64, 0, 0x10000
	s_add_i32 s65, 0, 0x14000
	ds_read_b128 v[4:7], v189
	ds_read_b128 v[8:11], v245
	ds_read_b128 v[12:15], v189 offset:2048
	ds_read_b128 v[16:19], v245 offset:2048
	ds_read_b128 v[20:23], v189 offset:16384
	ds_read_b128 v[24:27], v245 offset:16384
	ds_read_b128 v[28:31], v189 offset:18432
	ds_read_b128 v[32:35], v245 offset:18432
	s_add_u32 s34, s34, 0x10000
	s_addc_u32 s35, s35, 0
	v_lshl_add_u64 v[164:165], s[34:35], 0, v[178:179]
	s_add_i32 m0, s43, 0xc000
	ds_read_b128 v[180:183], v190
	ds_read_b128 v[184:187], v246
	ds_read_b128 v[192:195], v190 offset:2048
	ds_read_b128 v[196:199], v246 offset:2048
	ds_read_b128 v[200:203], v190 offset:4096
	ds_read_b128 v[204:207], v246 offset:4096
	ds_read_b128 v[226:229], v190 offset:6144
	ds_read_b128 v[230:233], v246 offset:6144
	global_load_lds_dwordx4 v[164:165], off
	v_lshl_add_u64 v[164:165], s[34:35], 0, v[174:175]
	s_add_i32 m0, s43, 0xe000
	s_nop 0
	global_load_lds_dwordx4 v[164:165], off
	s_waitcnt vmcnt(8)
	s_waitcnt lgkmcnt(0)
	s_barrier
	s_setprio 1
	v_mfma_f32_16x16x128_f8f6f4 v[160:163], v[4:11], v[180:187], v[160:163]
	v_mfma_f32_16x16x128_f8f6f4 v[156:159], v[12:19], v[180:187], v[156:159]
	v_mfma_f32_16x16x128_f8f6f4 v[144:147], v[4:11], v[192:199], v[144:147]
	v_mfma_f32_16x16x128_f8f6f4 v[140:143], v[12:19], v[192:199], v[140:143]
	v_mfma_f32_16x16x128_f8f6f4 v[128:131], v[4:11], v[200:207], v[128:131]
	v_mfma_f32_16x16x128_f8f6f4 v[124:127], v[12:19], v[200:207], v[124:127]
	v_mfma_f32_16x16x128_f8f6f4 v[112:115], v[4:11], v[226:233], v[112:115]
	v_mfma_f32_16x16x128_f8f6f4 v[108:111], v[12:19], v[226:233], v[108:111]
	v_mfma_f32_16x16x128_f8f6f4 v[152:155], v[20:27], v[180:187], v[152:155]
	v_mfma_f32_16x16x128_f8f6f4 v[148:151], v[28:35], v[180:187], v[148:151]
	v_mfma_f32_16x16x128_f8f6f4 v[136:139], v[20:27], v[192:199], v[136:139]
	v_mfma_f32_16x16x128_f8f6f4 v[132:135], v[28:35], v[192:199], v[132:135]
	v_mfma_f32_16x16x128_f8f6f4 v[120:123], v[20:27], v[200:207], v[120:123]
	v_mfma_f32_16x16x128_f8f6f4 v[116:119], v[28:35], v[200:207], v[116:119]
	v_mfma_f32_16x16x128_f8f6f4 v[104:107], v[20:27], v[226:233], v[104:107]
	v_mfma_f32_16x16x128_f8f6f4 v[100:103], v[28:35], v[226:233], v[100:103]
	s_setprio 0
	s_barrier
	s_add_i32 s34, s64, s42
	v_lshl_add_u64 v[182:183], s[36:37], 0, v[176:177]
	s_mov_b32 m0, s34
	ds_read_b128 v[192:195], v190 offset:16384
	ds_read_b128 v[196:199], v246 offset:16384
	ds_read_b128 v[200:203], v190 offset:18432
	ds_read_b128 v[204:207], v246 offset:18432
	ds_read_b128 v[226:229], v190 offset:20480
	ds_read_b128 v[230:233], v246 offset:20480
	ds_read_b128 v[234:237], v190 offset:22528
	ds_read_b128 v[238:241], v246 offset:22528
	global_load_lds_dwordx4 v[182:183], off
	s_add_i32 m0, s34, 0x2000
	s_add_u32 s34, s36, 0x10000
	v_lshl_add_u64 v[184:185], s[36:37], 0, v[172:173]
	s_addc_u32 s35, s37, 0
	s_add_i32 s64, s65, s42
	global_load_lds_dwordx4 v[184:185], off
	v_lshl_add_u64 v[164:165], s[34:35], 0, v[176:177]
	s_mov_b32 m0, s64
	v_lshl_add_u64 v[186:187], s[30:31], 0, v[178:179]
	global_load_lds_dwordx4 v[164:165], off
	v_lshl_add_u64 v[164:165], s[34:35], 0, v[172:173]
	s_add_i32 m0, s64, 0x2000
	v_lshl_add_u64 v[180:181], s[30:31], 0, v[174:175]
	global_load_lds_dwordx4 v[164:165], off
	s_mov_b32 m0, s43
	s_nop 0
	global_load_lds_dwordx4 v[186:187], off
	s_mov_b32 m0, s44
	s_nop 0
	global_load_lds_dwordx4 v[180:181], off
	s_waitcnt vmcnt(8)
	s_waitcnt lgkmcnt(0)
	s_barrier
	s_setprio 1
	v_mfma_f32_16x16x128_f8f6f4 v[96:99], v[4:11], v[192:199], v[96:99]
	v_mfma_f32_16x16x128_f8f6f4 v[92:95], v[12:19], v[192:199], v[92:95]
	v_mfma_f32_16x16x128_f8f6f4 v[80:83], v[4:11], v[200:207], v[80:83]
	v_mfma_f32_16x16x128_f8f6f4 v[76:79], v[12:19], v[200:207], v[76:79]
	v_mfma_f32_16x16x128_f8f6f4 v[64:67], v[4:11], v[226:233], v[64:67]
	v_mfma_f32_16x16x128_f8f6f4 v[60:63], v[12:19], v[226:233], v[60:63]
	v_mfma_f32_16x16x128_f8f6f4 v[48:51], v[4:11], v[234:241], v[48:51]
	v_mfma_f32_16x16x128_f8f6f4 v[44:47], v[12:19], v[234:241], v[44:47]
	v_mfma_f32_16x16x128_f8f6f4 v[88:91], v[20:27], v[192:199], v[88:91]
	v_mfma_f32_16x16x128_f8f6f4 v[84:87], v[28:35], v[192:199], v[84:87]
	v_mfma_f32_16x16x128_f8f6f4 v[72:75], v[20:27], v[200:207], v[72:75]
	v_mfma_f32_16x16x128_f8f6f4 v[68:71], v[28:35], v[200:207], v[68:71]
	v_mfma_f32_16x16x128_f8f6f4 v[56:59], v[20:27], v[226:233], v[56:59]
	v_mfma_f32_16x16x128_f8f6f4 v[52:55], v[28:35], v[226:233], v[52:55]
	v_mfma_f32_16x16x128_f8f6f4 v[40:43], v[20:27], v[234:241], v[40:43]
	v_mfma_f32_16x16x128_f8f6f4 v[36:39], v[28:35], v[234:241], v[36:39]
	s_setprio 0
	s_barrier
	s_add_i32 s34, 0, 0x18000
	s_add_i32 s35, 0, 0x1c000
	ds_read_b128 v[12:15], v189 offset:32768
	ds_read_b128 v[16:19], v245 offset:32768
	ds_read_b128 v[28:31], v189 offset:34816
	ds_read_b128 v[32:35], v245 offset:34816
	ds_read_b128 v[4:7], v189 offset:49152
	ds_read_b128 v[8:11], v245 offset:49152
	ds_read_b128 v[20:23], v189 offset:51200
	ds_read_b128 v[24:27], v245 offset:51200
	s_add_u32 s30, s30, 0x10000
	s_addc_u32 s31, s31, 0
	s_mov_b32 m0, s45
	v_lshl_add_u64 v[164:165], s[30:31], 0, v[178:179]
	ds_read_b128 v[192:195], v190 offset:32768
	ds_read_b128 v[196:199], v246 offset:32768
	ds_read_b128 v[200:203], v190 offset:34816
	ds_read_b128 v[204:207], v246 offset:34816
	ds_read_b128 v[226:229], v190 offset:36864
	ds_read_b128 v[230:233], v246 offset:36864
	ds_read_b128 v[234:237], v190 offset:38912
	ds_read_b128 v[238:241], v246 offset:38912
	global_load_lds_dwordx4 v[164:165], off
	v_lshl_add_u64 v[164:165], s[30:31], 0, v[174:175]
	s_mov_b32 m0, s46
	s_nop 0
	global_load_lds_dwordx4 v[164:165], off
	s_waitcnt vmcnt(8)
	s_waitcnt lgkmcnt(0)
	s_barrier
	s_setprio 1
	v_mfma_f32_16x16x128_f8f6f4 v[160:163], v[12:19], v[192:199], v[160:163]
	v_mfma_f32_16x16x128_f8f6f4 v[156:159], v[28:35], v[192:199], v[156:159]
	v_mfma_f32_16x16x128_f8f6f4 v[144:147], v[12:19], v[200:207], v[144:147]
	v_mfma_f32_16x16x128_f8f6f4 v[140:143], v[28:35], v[200:207], v[140:143]
	v_mfma_f32_16x16x128_f8f6f4 v[128:131], v[12:19], v[226:233], v[128:131]
	v_mfma_f32_16x16x128_f8f6f4 v[124:127], v[28:35], v[226:233], v[124:127]
	v_mfma_f32_16x16x128_f8f6f4 v[112:115], v[12:19], v[234:241], v[112:115]
	v_mfma_f32_16x16x128_f8f6f4 v[108:111], v[28:35], v[234:241], v[108:111]
	v_mfma_f32_16x16x128_f8f6f4 v[152:155], v[4:11], v[192:199], v[152:155]
	v_mfma_f32_16x16x128_f8f6f4 v[148:151], v[20:27], v[192:199], v[148:151]
	v_mfma_f32_16x16x128_f8f6f4 v[136:139], v[4:11], v[200:207], v[136:139]
	v_mfma_f32_16x16x128_f8f6f4 v[132:135], v[20:27], v[200:207], v[132:135]
	v_mfma_f32_16x16x128_f8f6f4 v[120:123], v[4:11], v[226:233], v[120:123]
	v_mfma_f32_16x16x128_f8f6f4 v[116:119], v[20:27], v[226:233], v[116:119]
	v_mfma_f32_16x16x128_f8f6f4 v[104:107], v[4:11], v[234:241], v[104:107]
	v_mfma_f32_16x16x128_f8f6f4 v[100:103], v[20:27], v[234:241], v[100:103]
	s_setprio 0
	s_barrier
	s_mov_b64 s[64:65], 0x80
	s_add_i32 s30, s34, s42
	v_lshl_add_u64 v[164:165], v[182:183], 0, s[64:65]
	s_mov_b32 m0, s30
	ds_read_b128 v[192:195], v190 offset:49152
	ds_read_b128 v[196:199], v246 offset:49152
	ds_read_b128 v[200:203], v190 offset:51200
	ds_read_b128 v[204:207], v246 offset:51200
	ds_read_b128 v[226:229], v190 offset:53248
	ds_read_b128 v[230:233], v246 offset:53248
	ds_read_b128 v[234:237], v190 offset:55296
	ds_read_b128 v[238:241], v246 offset:55296
	global_load_lds_dwordx4 v[164:165], off
	s_add_i32 m0, s30, 0x2000
	s_add_u32 s30, s36, 0x10080
	v_lshl_add_u64 v[164:165], v[184:185], 0, s[64:65]
	s_addc_u32 s31, s37, 0
	s_add_i32 s34, s35, s42
	global_load_lds_dwordx4 v[164:165], off
	v_lshl_add_u64 v[164:165], s[30:31], 0, v[176:177]
	s_mov_b32 m0, s34
	s_nop 0
	global_load_lds_dwordx4 v[164:165], off
	v_lshl_add_u64 v[164:165], s[30:31], 0, v[172:173]
	s_add_i32 m0, s34, 0x2000
	s_nop 0
	global_load_lds_dwordx4 v[164:165], off
	v_lshl_add_u64 v[164:165], v[186:187], 0, s[64:65]
	s_mov_b32 m0, s53
	s_nop 0
	global_load_lds_dwordx4 v[164:165], off
	v_lshl_add_u64 v[164:165], v[180:181], 0, s[64:65]
	s_mov_b32 m0, s54
	s_nop 0
	global_load_lds_dwordx4 v[164:165], off
	s_waitcnt vmcnt(8)
	s_waitcnt lgkmcnt(0)
	s_barrier
	s_setprio 1
	v_mfma_f32_16x16x128_f8f6f4 v[96:99], v[12:19], v[192:199], v[96:99]
	v_mfma_f32_16x16x128_f8f6f4 v[92:95], v[28:35], v[192:199], v[92:95]
	v_mfma_f32_16x16x128_f8f6f4 v[80:83], v[12:19], v[200:207], v[80:83]
	v_mfma_f32_16x16x128_f8f6f4 v[76:79], v[28:35], v[200:207], v[76:79]
	v_mfma_f32_16x16x128_f8f6f4 v[64:67], v[12:19], v[226:233], v[64:67]
	v_mfma_f32_16x16x128_f8f6f4 v[60:63], v[28:35], v[226:233], v[60:63]
	v_mfma_f32_16x16x128_f8f6f4 v[48:51], v[12:19], v[234:241], v[48:51]
	v_mfma_f32_16x16x128_f8f6f4 v[44:47], v[28:35], v[234:241], v[44:47]
	v_mfma_f32_16x16x128_f8f6f4 v[88:91], v[4:11], v[192:199], v[88:91]
	v_mfma_f32_16x16x128_f8f6f4 v[84:87], v[20:27], v[192:199], v[84:87]
	v_mfma_f32_16x16x128_f8f6f4 v[72:75], v[4:11], v[200:207], v[72:75]
	v_mfma_f32_16x16x128_f8f6f4 v[68:71], v[20:27], v[200:207], v[68:71]
	v_mfma_f32_16x16x128_f8f6f4 v[56:59], v[4:11], v[226:233], v[56:59]
	v_mfma_f32_16x16x128_f8f6f4 v[52:55], v[20:27], v[226:233], v[52:55]
	v_mfma_f32_16x16x128_f8f6f4 v[40:43], v[4:11], v[234:241], v[40:43]
	v_mfma_f32_16x16x128_f8f6f4 v[36:39], v[20:27], v[234:241], v[36:39]
	s_setprio 0
	s_barrier
	s_mov_b64 s[64:65], s[72:73]
	s_add_i32 s64, s64, 2
	s_add_u32 s28, s28, 0x100
	s_addc_u32 s29, s29, 0
	s_cmp_gt_u32 s63, 5
	s_cbranch_scc1 .LBB0_632

.LBB0_702:
	s_add_u32 s18, s0, 0xffed0080
	s_addc_u32 s19, s1, -1
	s_add_i32 s47, 0, 0x10000
	s_cmp_eq_u32 s46, 4
	s_cselect_b32 s21, s15, s19
	s_cselect_b32 s20, s14, s18
	s_cselect_b32 s19, s13, s45
	s_cselect_b32 s18, s43, s44
	s_add_i32 s48, 0, 0x14000
	ds_read_b128 v[20:23], v226
	ds_read_b128 v[24:27], v245
	ds_read_b128 v[28:31], v226 offset:2048
	ds_read_b128 v[32:35], v245 offset:2048
	ds_read_b128 v[4:7], v226 offset:16384
	ds_read_b128 v[8:11], v245 offset:16384
	ds_read_b128 v[12:15], v226 offset:18432
	ds_read_b128 v[16:19], v245 offset:18432
	v_lshl_add_u64 v[164:165], s[0:1], 0, v[180:181]
	s_add_i32 m0, s27, 0xc000
	ds_read_b128 v[184:187], v227
	ds_read_b128 v[188:191], v246
	ds_read_b128 v[192:195], v227 offset:2048
	ds_read_b128 v[196:199], v246 offset:2048
	ds_read_b128 v[200:203], v227 offset:4096
	ds_read_b128 v[204:207], v246 offset:4096
	ds_read_b128 v[228:231], v227 offset:6144
	ds_read_b128 v[232:235], v246 offset:6144
	global_load_lds_dwordx4 v[164:165], off
	v_lshl_add_u64 v[164:165], s[0:1], 0, v[182:183]
	s_add_i32 m0, s27, 0xe000
	s_nop 0
	global_load_lds_dwordx4 v[164:165], off
	s_waitcnt vmcnt(8)
	s_waitcnt lgkmcnt(0)
	s_barrier
	s_setprio 1
	v_mfma_f32_16x16x128_f8f6f4 v[160:163], v[20:27], v[184:191], v[160:163]
	v_mfma_f32_16x16x128_f8f6f4 v[156:159], v[28:35], v[184:191], v[156:159]
	v_mfma_f32_16x16x128_f8f6f4 v[144:147], v[20:27], v[192:199], v[144:147]
	v_mfma_f32_16x16x128_f8f6f4 v[140:143], v[28:35], v[192:199], v[140:143]
	v_mfma_f32_16x16x128_f8f6f4 v[128:131], v[20:27], v[200:207], v[128:131]
	v_mfma_f32_16x16x128_f8f6f4 v[124:127], v[28:35], v[200:207], v[124:127]
	v_mfma_f32_16x16x128_f8f6f4 v[112:115], v[20:27], v[228:235], v[112:115]
	v_mfma_f32_16x16x128_f8f6f4 v[108:111], v[28:35], v[228:235], v[108:111]
	v_mfma_f32_16x16x128_f8f6f4 v[152:155], v[4:11], v[184:191], v[152:155]
	v_mfma_f32_16x16x128_f8f6f4 v[148:151], v[12:19], v[184:191], v[148:151]
	v_mfma_f32_16x16x128_f8f6f4 v[136:139], v[4:11], v[192:199], v[136:139]
	v_mfma_f32_16x16x128_f8f6f4 v[132:135], v[12:19], v[192:199], v[132:135]
	v_mfma_f32_16x16x128_f8f6f4 v[120:123], v[4:11], v[200:207], v[120:123]
	v_mfma_f32_16x16x128_f8f6f4 v[116:119], v[12:19], v[200:207], v[116:119]
	v_mfma_f32_16x16x128_f8f6f4 v[104:107], v[4:11], v[228:235], v[104:107]
	v_mfma_f32_16x16x128_f8f6f4 v[100:103], v[12:19], v[228:235], v[100:103]
	s_setprio 0
	s_barrier
	s_add_i32 s47, s47, s26
	v_lshl_add_u64 v[184:185], s[18:19], 0, v[176:177]
	s_mov_b32 m0, s47
	ds_read_b128 v[192:195], v227 offset:16384
	ds_read_b128 v[196:199], v246 offset:16384
	ds_read_b128 v[200:203], v227 offset:18432
	ds_read_b128 v[204:207], v246 offset:18432
	ds_read_b128 v[228:231], v227 offset:20480
	ds_read_b128 v[232:235], v246 offset:20480
	ds_read_b128 v[236:239], v227 offset:22528
	ds_read_b128 v[240:243], v246 offset:22528
	global_load_lds_dwordx4 v[184:185], off
	s_add_i32 m0, s47, 0x2000
	s_add_u32 s50, s18, 0x20000
	v_lshl_add_u64 v[186:187], s[18:19], 0, v[172:173]
	s_addc_u32 s51, s19, 0
	s_add_i32 s47, s48, s26
	global_load_lds_dwordx4 v[186:187], off
	v_lshl_add_u64 v[164:165], s[50:51], 0, v[176:177]
	s_mov_b32 m0, s47
	v_lshl_add_u64 v[188:189], s[20:21], 0, v[178:179]
	global_load_lds_dwordx4 v[164:165], off
	v_lshl_add_u64 v[164:165], s[50:51], 0, v[172:173]
	s_add_i32 m0, s47, 0x2000
	v_lshl_add_u64 v[190:191], s[20:21], 0, v[174:175]
	global_load_lds_dwordx4 v[164:165], off
	s_mov_b32 m0, s27
	s_nop 0
	global_load_lds_dwordx4 v[188:189], off
	s_mov_b32 m0, s28
	s_nop 0
	global_load_lds_dwordx4 v[190:191], off
	s_waitcnt vmcnt(8)
	s_waitcnt lgkmcnt(0)
	s_barrier
	s_setprio 1
	v_mfma_f32_16x16x128_f8f6f4 v[96:99], v[20:27], v[192:199], v[96:99]
	v_mfma_f32_16x16x128_f8f6f4 v[92:95], v[28:35], v[192:199], v[92:95]
	v_mfma_f32_16x16x128_f8f6f4 v[80:83], v[20:27], v[200:207], v[80:83]
	v_mfma_f32_16x16x128_f8f6f4 v[76:79], v[28:35], v[200:207], v[76:79]
	v_mfma_f32_16x16x128_f8f6f4 v[64:67], v[20:27], v[228:235], v[64:67]
	v_mfma_f32_16x16x128_f8f6f4 v[60:63], v[28:35], v[228:235], v[60:63]
	v_mfma_f32_16x16x128_f8f6f4 v[48:51], v[20:27], v[236:243], v[48:51]
	v_mfma_f32_16x16x128_f8f6f4 v[44:47], v[28:35], v[236:243], v[44:47]
	v_mfma_f32_16x16x128_f8f6f4 v[88:91], v[4:11], v[192:199], v[88:91]
	v_mfma_f32_16x16x128_f8f6f4 v[84:87], v[12:19], v[192:199], v[84:87]
	v_mfma_f32_16x16x128_f8f6f4 v[72:75], v[4:11], v[200:207], v[72:75]
	v_mfma_f32_16x16x128_f8f6f4 v[68:71], v[12:19], v[200:207], v[68:71]
	v_mfma_f32_16x16x128_f8f6f4 v[56:59], v[4:11], v[228:235], v[56:59]
	v_mfma_f32_16x16x128_f8f6f4 v[52:55], v[12:19], v[228:235], v[52:55]
	v_mfma_f32_16x16x128_f8f6f4 v[40:43], v[4:11], v[236:243], v[40:43]
	v_mfma_f32_16x16x128_f8f6f4 v[36:39], v[12:19], v[236:243], v[36:39]
	s_setprio 0
	s_barrier
	s_add_i32 s47, 0, 0x18000
	s_add_i32 s48, 0, 0x1c000
	ds_read_b128 v[4:7], v226 offset:32768
	ds_read_b128 v[8:11], v245 offset:32768
	ds_read_b128 v[12:15], v226 offset:34816
	ds_read_b128 v[16:19], v245 offset:34816
	ds_read_b128 v[20:23], v226 offset:49152
	ds_read_b128 v[24:27], v245 offset:49152
	ds_read_b128 v[28:31], v226 offset:51200
	ds_read_b128 v[32:35], v245 offset:51200
	s_add_u32 s20, s20, 0x130000
	s_addc_u32 s21, s21, 0
	s_mov_b32 m0, s29
	v_lshl_add_u64 v[164:165], s[20:21], 0, v[178:179]
	ds_read_b128 v[192:195], v227 offset:32768
	ds_read_b128 v[196:199], v246 offset:32768
	ds_read_b128 v[200:203], v227 offset:34816
	ds_read_b128 v[204:207], v246 offset:34816
	ds_read_b128 v[228:231], v227 offset:36864
	ds_read_b128 v[232:235], v246 offset:36864
	ds_read_b128 v[236:239], v227 offset:38912
	ds_read_b128 v[240:243], v246 offset:38912
	global_load_lds_dwordx4 v[164:165], off
	v_lshl_add_u64 v[164:165], s[20:21], 0, v[174:175]
	s_mov_b32 m0, s30
	s_nop 0
	global_load_lds_dwordx4 v[164:165], off
	s_waitcnt vmcnt(8)
	s_waitcnt lgkmcnt(0)
	s_barrier
	s_setprio 1
	v_mfma_f32_16x16x128_f8f6f4 v[160:163], v[4:11], v[192:199], v[160:163]
	v_mfma_f32_16x16x128_f8f6f4 v[156:159], v[12:19], v[192:199], v[156:159]
	v_mfma_f32_16x16x128_f8f6f4 v[144:147], v[4:11], v[200:207], v[144:147]
	v_mfma_f32_16x16x128_f8f6f4 v[140:143], v[12:19], v[200:207], v[140:143]
	v_mfma_f32_16x16x128_f8f6f4 v[128:131], v[4:11], v[228:235], v[128:131]
	v_mfma_f32_16x16x128_f8f6f4 v[124:127], v[12:19], v[228:235], v[124:127]
	v_mfma_f32_16x16x128_f8f6f4 v[112:115], v[4:11], v[236:243], v[112:115]
	v_mfma_f32_16x16x128_f8f6f4 v[108:111], v[12:19], v[236:243], v[108:111]
	v_mfma_f32_16x16x128_f8f6f4 v[152:155], v[20:27], v[192:199], v[152:155]
	v_mfma_f32_16x16x128_f8f6f4 v[148:151], v[28:35], v[192:199], v[148:151]
	v_mfma_f32_16x16x128_f8f6f4 v[136:139], v[20:27], v[200:207], v[136:139]
	v_mfma_f32_16x16x128_f8f6f4 v[132:135], v[28:35], v[200:207], v[132:135]
	v_mfma_f32_16x16x128_f8f6f4 v[120:123], v[20:27], v[228:235], v[120:123]
	v_mfma_f32_16x16x128_f8f6f4 v[116:119], v[28:35], v[228:235], v[116:119]
	v_mfma_f32_16x16x128_f8f6f4 v[104:107], v[20:27], v[236:243], v[104:107]
	v_mfma_f32_16x16x128_f8f6f4 v[100:103], v[28:35], v[236:243], v[100:103]
	s_setprio 0
	s_barrier
	s_add_i32 s20, s47, s26
	v_lshl_add_u64 v[164:165], v[184:185], 0, s[52:53]
	s_mov_b32 m0, s20
	ds_read_b128 v[192:195], v227 offset:49152
	ds_read_b128 v[196:199], v246 offset:49152
	ds_read_b128 v[200:203], v227 offset:51200
	ds_read_b128 v[204:207], v246 offset:51200
	ds_read_b128 v[228:231], v227 offset:53248
	ds_read_b128 v[232:235], v246 offset:53248
	ds_read_b128 v[236:239], v227 offset:55296
	ds_read_b128 v[240:243], v246 offset:55296
	global_load_lds_dwordx4 v[164:165], off
	s_add_i32 m0, s20, 0x2000
	s_add_u32 s18, s18, 0x20080
	v_lshl_add_u64 v[164:165], v[186:187], 0, s[52:53]
	s_addc_u32 s19, s19, 0
	s_add_i32 s20, s48, s26
	global_load_lds_dwordx4 v[164:165], off
	v_lshl_add_u64 v[164:165], s[18:19], 0, v[176:177]
	s_mov_b32 m0, s20
	s_nop 0
	global_load_lds_dwordx4 v[164:165], off
	v_lshl_add_u64 v[164:165], s[18:19], 0, v[172:173]
	s_add_i32 m0, s20, 0x2000
	s_nop 0
	global_load_lds_dwordx4 v[164:165], off
	v_lshl_add_u64 v[164:165], v[188:189], 0, s[52:53]
	s_mov_b32 m0, s38
	s_nop 0
	global_load_lds_dwordx4 v[164:165], off
	v_lshl_add_u64 v[164:165], v[190:191], 0, s[52:53]
	s_mov_b32 m0, s39
	s_nop 0
	global_load_lds_dwordx4 v[164:165], off
	s_waitcnt vmcnt(8)
	s_waitcnt lgkmcnt(0)
	s_barrier
	s_setprio 1
	v_mfma_f32_16x16x128_f8f6f4 v[96:99], v[4:11], v[192:199], v[96:99]
	v_mfma_f32_16x16x128_f8f6f4 v[92:95], v[12:19], v[192:199], v[92:95]
	v_mfma_f32_16x16x128_f8f6f4 v[80:83], v[4:11], v[200:207], v[80:83]
	v_mfma_f32_16x16x128_f8f6f4 v[76:79], v[12:19], v[200:207], v[76:79]
	v_mfma_f32_16x16x128_f8f6f4 v[64:67], v[4:11], v[228:235], v[64:67]
	v_mfma_f32_16x16x128_f8f6f4 v[60:63], v[12:19], v[228:235], v[60:63]
	v_mfma_f32_16x16x128_f8f6f4 v[48:51], v[4:11], v[236:243], v[48:51]
	v_mfma_f32_16x16x128_f8f6f4 v[44:47], v[12:19], v[236:243], v[44:47]
	v_mfma_f32_16x16x128_f8f6f4 v[88:91], v[20:27], v[192:199], v[88:91]
	v_mfma_f32_16x16x128_f8f6f4 v[84:87], v[28:35], v[192:199], v[84:87]
	v_mfma_f32_16x16x128_f8f6f4 v[72:75], v[20:27], v[200:207], v[72:75]
	v_mfma_f32_16x16x128_f8f6f4 v[68:71], v[28:35], v[200:207], v[68:71]
	v_mfma_f32_16x16x128_f8f6f4 v[56:59], v[20:27], v[228:235], v[56:59]
	v_mfma_f32_16x16x128_f8f6f4 v[52:55], v[28:35], v[228:235], v[52:55]
	v_mfma_f32_16x16x128_f8f6f4 v[40:43], v[20:27], v[236:243], v[40:43]
	v_mfma_f32_16x16x128_f8f6f4 v[36:39], v[28:35], v[236:243], v[36:39]
	s_setprio 0
	s_barrier
	s_add_i32 s46, s46, 2
	s_add_u32 s0, s0, 0x100
	s_addc_u32 s1, s1, 0
	s_add_u32 s44, s44, 0x100
	s_addc_u32 s45, s45, 0
	s_cmp_gt_u32 s46, 5
	s_cbranch_scc0 .LBB0_702
	s_and_b64 vcc, exec, s[10:11]
	s_cbranch_vccz .LBB0_705
	s_barrier

.LBB0_879:
	s_add_u32 s38, s34, 0x80
	s_addc_u32 s39, s35, 0
	s_add_i32 s66, 0, 0x10000
	s_cmp_eq_u32 s65, 4
	s_cselect_b64 vcc, -1, 0
	s_and_b64 s[36:37], vcc, exec
	s_cselect_b32 s39, s1, s39
	s_cselect_b32 s38, s0, s38
	s_cselect_b32 s37, s29, s64
	s_cselect_b32 s36, s28, s63
	s_add_i32 s67, 0, 0x14000
	ds_read_b128 v[20:23], v192
	ds_read_b128 v[24:27], v207
	ds_read_b128 v[28:31], v192 offset:2048
	ds_read_b128 v[32:35], v207 offset:2048
	ds_read_b128 v[4:7], v192 offset:16384
	ds_read_b128 v[8:11], v207 offset:16384
	ds_read_b128 v[12:15], v192 offset:18432
	ds_read_b128 v[16:19], v207 offset:18432
	v_lshl_add_u64 v[164:165], s[34:35], 0, v[178:179]
	s_add_i32 m0, s47, 0xc000
	ds_read_b128 v[182:185], v193
	ds_read_b128 v[186:189], v208
	ds_read_b128 v[198:201], v193 offset:2048
	ds_read_b128 v[202:205], v208 offset:2048
	ds_read_b128 v[226:229], v193 offset:4096
	ds_read_b128 v[230:233], v208 offset:4096
	ds_read_b128 v[234:237], v193 offset:6144
	ds_read_b128 v[238:241], v208 offset:6144
	global_load_lds_dwordx4 v[164:165], off
	v_lshl_add_u64 v[164:165], s[34:35], 0, v[180:181]
	s_add_i32 m0, s47, 0xe000
	s_nop 0
	global_load_lds_dwordx4 v[164:165], off
	s_waitcnt vmcnt(8)
	s_waitcnt lgkmcnt(0)
	s_barrier
	s_setprio 1
	v_mfma_f32_16x16x128_f8f6f4 v[160:163], v[20:27], v[182:189], v[160:163]
	v_mfma_f32_16x16x128_f8f6f4 v[156:159], v[28:35], v[182:189], v[156:159]
	v_mfma_f32_16x16x128_f8f6f4 v[144:147], v[20:27], v[198:205], v[144:147]
	v_mfma_f32_16x16x128_f8f6f4 v[140:143], v[28:35], v[198:205], v[140:143]
	v_mfma_f32_16x16x128_f8f6f4 v[128:131], v[20:27], v[226:233], v[128:131]
	v_mfma_f32_16x16x128_f8f6f4 v[124:127], v[28:35], v[226:233], v[124:127]
	v_mfma_f32_16x16x128_f8f6f4 v[112:115], v[20:27], v[234:241], v[112:115]
	v_mfma_f32_16x16x128_f8f6f4 v[108:111], v[28:35], v[234:241], v[108:111]
	v_mfma_f32_16x16x128_f8f6f4 v[152:155], v[4:11], v[182:189], v[152:155]
	v_mfma_f32_16x16x128_f8f6f4 v[148:151], v[12:19], v[182:189], v[148:151]
	v_mfma_f32_16x16x128_f8f6f4 v[136:139], v[4:11], v[198:205], v[136:139]
	v_mfma_f32_16x16x128_f8f6f4 v[132:135], v[12:19], v[198:205], v[132:135]
	v_mfma_f32_16x16x128_f8f6f4 v[120:123], v[4:11], v[226:233], v[120:123]
	v_mfma_f32_16x16x128_f8f6f4 v[116:119], v[12:19], v[226:233], v[116:119]
	v_mfma_f32_16x16x128_f8f6f4 v[104:107], v[4:11], v[234:241], v[104:107]
	v_mfma_f32_16x16x128_f8f6f4 v[100:103], v[12:19], v[234:241], v[100:103]
	s_setprio 0
	s_barrier
	s_add_i32 s66, s66, s46
	v_lshl_add_u64 v[182:183], s[36:37], 0, v[176:177]
	s_mov_b32 m0, s66
	ds_read_b128 v[198:201], v193 offset:16384
	ds_read_b128 v[202:205], v208 offset:16384
	ds_read_b128 v[226:229], v193 offset:18432
	ds_read_b128 v[230:233], v208 offset:18432
	ds_read_b128 v[234:237], v193 offset:20480
	ds_read_b128 v[238:241], v208 offset:20480
	ds_read_b128 v[242:245], v193 offset:22528
	ds_read_b128 v[246:249], v208 offset:22528
	global_load_lds_dwordx4 v[182:183], off
	s_add_i32 m0, s66, 0x2000
	s_add_u32 s68, s36, 0x20000
	v_lshl_add_u64 v[184:185], s[36:37], 0, v[174:175]
	s_addc_u32 s69, s37, 0
	s_add_i32 s66, s67, s46
	global_load_lds_dwordx4 v[184:185], off
	v_lshl_add_u64 v[164:165], s[68:69], 0, v[176:177]
	s_mov_b32 m0, s66
	v_mov_b32_e32 v167, v2
	global_load_lds_dwordx4 v[164:165], off
	v_lshl_add_u64 v[164:165], s[68:69], 0, v[174:175]
	s_add_i32 m0, s66, 0x2000
	s_nop 0
	global_load_lds_dwordx4 v[164:165], off
	v_cndmask_b32_e32 v165, v196, v194, vcc
	v_lshlrev_b32_e32 v164, 10, v165
	v_and_b32_e32 v164, 0x3fffc00, v164
	v_add_u32_e32 v164, v164, v1
	s_mov_b32 m0, s47
	v_bfe_u32 v165, v165, 16, 16
	global_load_lds_dwordx4 v164, s[38:39]
	v_lshl_add_u32 v166, v165, 10, v1
	s_mov_b32 m0, s48
	v_mov_b32_e32 v165, v2
	global_load_lds_dwordx4 v166, s[38:39]
	s_waitcnt vmcnt(8)
	s_waitcnt lgkmcnt(0)
	v_lshl_add_u64 v[188:189], s[38:39], 0, v[164:165]
	v_lshl_add_u64 v[186:187], s[38:39], 0, v[166:167]
	s_barrier
	s_setprio 1
	v_mfma_f32_16x16x128_f8f6f4 v[96:99], v[20:27], v[198:205], v[96:99]
	v_mfma_f32_16x16x128_f8f6f4 v[92:95], v[28:35], v[198:205], v[92:95]
	v_mfma_f32_16x16x128_f8f6f4 v[80:83], v[20:27], v[226:233], v[80:83]
	v_mfma_f32_16x16x128_f8f6f4 v[76:79], v[28:35], v[226:233], v[76:79]
	v_mfma_f32_16x16x128_f8f6f4 v[64:67], v[20:27], v[234:241], v[64:67]
	v_mfma_f32_16x16x128_f8f6f4 v[60:63], v[28:35], v[234:241], v[60:63]
	v_mfma_f32_16x16x128_f8f6f4 v[48:51], v[20:27], v[242:249], v[48:51]
	v_mfma_f32_16x16x128_f8f6f4 v[44:47], v[28:35], v[242:249], v[44:47]
	v_mfma_f32_16x16x128_f8f6f4 v[88:91], v[4:11], v[198:205], v[88:91]
	v_mfma_f32_16x16x128_f8f6f4 v[84:87], v[12:19], v[198:205], v[84:87]
	v_mfma_f32_16x16x128_f8f6f4 v[72:75], v[4:11], v[226:233], v[72:75]
	v_mfma_f32_16x16x128_f8f6f4 v[68:71], v[12:19], v[226:233], v[68:71]
	v_mfma_f32_16x16x128_f8f6f4 v[56:59], v[4:11], v[234:241], v[56:59]
	v_mfma_f32_16x16x128_f8f6f4 v[52:55], v[12:19], v[234:241], v[52:55]
	v_mfma_f32_16x16x128_f8f6f4 v[40:43], v[4:11], v[242:249], v[40:43]
	v_mfma_f32_16x16x128_f8f6f4 v[36:39], v[12:19], v[242:249], v[36:39]
	s_setprio 0
	s_barrier
	s_add_i32 s66, 0, 0x18000
	s_add_i32 s67, 0, 0x1c000
	ds_read_b128 v[4:7], v192 offset:32768
	ds_read_b128 v[8:11], v207 offset:32768
	ds_read_b128 v[12:15], v192 offset:34816
	ds_read_b128 v[16:19], v207 offset:34816
	ds_read_b128 v[20:23], v192 offset:49152
	ds_read_b128 v[24:27], v207 offset:49152
	ds_read_b128 v[28:31], v192 offset:51200
	ds_read_b128 v[32:35], v207 offset:51200
	v_cndmask_b32_e32 v164, v170, v195, vcc
	v_lshlrev_b32_e32 v165, 10, v164
	v_and_b32_e32 v165, 0x3fffc00, v165
	s_mov_b32 m0, s49
	v_add_u32_e32 v165, v165, v1
	v_bfe_u32 v164, v164, 16, 16
	ds_read_b128 v[198:201], v193 offset:32768
	ds_read_b128 v[202:205], v208 offset:32768
	ds_read_b128 v[226:229], v193 offset:34816
	ds_read_b128 v[230:233], v208 offset:34816
	ds_read_b128 v[234:237], v193 offset:36864
	ds_read_b128 v[238:241], v208 offset:36864
	ds_read_b128 v[242:245], v193 offset:38912
	ds_read_b128 v[246:249], v208 offset:38912
	global_load_lds_dwordx4 v165, s[38:39]
	v_lshl_add_u32 v164, v164, 10, v1
	s_mov_b32 m0, s50
	s_nop 0
	global_load_lds_dwordx4 v164, s[38:39]
	s_waitcnt vmcnt(8)
	s_waitcnt lgkmcnt(0)
	s_barrier
	s_setprio 1
	v_mfma_f32_16x16x128_f8f6f4 v[160:163], v[4:11], v[198:205], v[160:163]
	v_mfma_f32_16x16x128_f8f6f4 v[156:159], v[12:19], v[198:205], v[156:159]
	v_mfma_f32_16x16x128_f8f6f4 v[144:147], v[4:11], v[226:233], v[144:147]
	v_mfma_f32_16x16x128_f8f6f4 v[140:143], v[12:19], v[226:233], v[140:143]
	v_mfma_f32_16x16x128_f8f6f4 v[128:131], v[4:11], v[234:241], v[128:131]
	v_mfma_f32_16x16x128_f8f6f4 v[124:127], v[12:19], v[234:241], v[124:127]
	v_mfma_f32_16x16x128_f8f6f4 v[112:115], v[4:11], v[242:249], v[112:115]
	v_mfma_f32_16x16x128_f8f6f4 v[108:111], v[12:19], v[242:249], v[108:111]
	v_mfma_f32_16x16x128_f8f6f4 v[152:155], v[20:27], v[198:205], v[152:155]
	v_mfma_f32_16x16x128_f8f6f4 v[148:151], v[28:35], v[198:205], v[148:151]
	v_mfma_f32_16x16x128_f8f6f4 v[136:139], v[20:27], v[226:233], v[136:139]
	v_mfma_f32_16x16x128_f8f6f4 v[132:135], v[28:35], v[226:233], v[132:135]
	v_mfma_f32_16x16x128_f8f6f4 v[120:123], v[20:27], v[234:241], v[120:123]
	v_mfma_f32_16x16x128_f8f6f4 v[116:119], v[28:35], v[234:241], v[116:119]
	v_mfma_f32_16x16x128_f8f6f4 v[104:107], v[20:27], v[242:249], v[104:107]
	v_mfma_f32_16x16x128_f8f6f4 v[100:103], v[28:35], v[242:249], v[100:103]
	s_setprio 0
	s_barrier
	s_add_i32 s38, s66, s46
	v_lshl_add_u64 v[164:165], v[182:183], 0, s[70:71]
	s_mov_b32 m0, s38
	ds_read_b128 v[198:201], v193 offset:49152
	ds_read_b128 v[202:205], v208 offset:49152
	ds_read_b128 v[226:229], v193 offset:51200
	ds_read_b128 v[230:233], v208 offset:51200
	ds_read_b128 v[234:237], v193 offset:53248
	ds_read_b128 v[238:241], v208 offset:53248
	ds_read_b128 v[242:245], v193 offset:55296
	ds_read_b128 v[246:249], v208 offset:55296
	global_load_lds_dwordx4 v[164:165], off
	s_add_i32 m0, s38, 0x2000
	s_add_u32 s36, s36, 0x20080
	v_lshl_add_u64 v[164:165], v[184:185], 0, s[70:71]
	s_addc_u32 s37, s37, 0
	s_add_i32 s38, s67, s46
	global_load_lds_dwordx4 v[164:165], off
	v_lshl_add_u64 v[164:165], s[36:37], 0, v[176:177]
	s_mov_b32 m0, s38
	s_nop 0
	global_load_lds_dwordx4 v[164:165], off
	v_lshl_add_u64 v[164:165], s[36:37], 0, v[174:175]
	s_add_i32 m0, s38, 0x2000
	s_nop 0
	global_load_lds_dwordx4 v[164:165], off
	v_lshl_add_u64 v[164:165], v[188:189], 0, s[70:71]
	s_mov_b32 m0, s55
	s_nop 0
	global_load_lds_dwordx4 v[164:165], off
	v_lshl_add_u64 v[164:165], v[186:187], 0, s[70:71]
	s_mov_b32 m0, s56
	s_nop 0
	global_load_lds_dwordx4 v[164:165], off
	s_waitcnt vmcnt(8)
	s_waitcnt lgkmcnt(0)
	s_barrier
	s_setprio 1
	v_mfma_f32_16x16x128_f8f6f4 v[96:99], v[4:11], v[198:205], v[96:99]
	v_mfma_f32_16x16x128_f8f6f4 v[92:95], v[12:19], v[198:205], v[92:95]
	v_mfma_f32_16x16x128_f8f6f4 v[80:83], v[4:11], v[226:233], v[80:83]
	v_mfma_f32_16x16x128_f8f6f4 v[76:79], v[12:19], v[226:233], v[76:79]
	v_mfma_f32_16x16x128_f8f6f4 v[64:67], v[4:11], v[234:241], v[64:67]
	v_mfma_f32_16x16x128_f8f6f4 v[60:63], v[12:19], v[234:241], v[60:63]
	v_mfma_f32_16x16x128_f8f6f4 v[48:51], v[4:11], v[242:249], v[48:51]
	v_mfma_f32_16x16x128_f8f6f4 v[44:47], v[12:19], v[242:249], v[44:47]
	v_mfma_f32_16x16x128_f8f6f4 v[88:91], v[20:27], v[198:205], v[88:91]
	v_mfma_f32_16x16x128_f8f6f4 v[84:87], v[28:35], v[198:205], v[84:87]
	v_mfma_f32_16x16x128_f8f6f4 v[72:75], v[20:27], v[226:233], v[72:75]
	v_mfma_f32_16x16x128_f8f6f4 v[68:71], v[28:35], v[226:233], v[68:71]
	v_mfma_f32_16x16x128_f8f6f4 v[56:59], v[20:27], v[234:241], v[56:59]
	v_mfma_f32_16x16x128_f8f6f4 v[52:55], v[28:35], v[234:241], v[52:55]
	v_mfma_f32_16x16x128_f8f6f4 v[40:43], v[20:27], v[242:249], v[40:43]
	v_mfma_f32_16x16x128_f8f6f4 v[36:39], v[28:35], v[242:249], v[36:39]
	s_setprio 0
	s_barrier
	s_add_i32 s65, s65, 2
	s_add_u32 s34, s34, 0x100
	s_addc_u32 s35, s35, 0
	s_add_u32 s63, s63, 0x100
	s_addc_u32 s64, s64, 0
	s_cmp_gt_u32 s65, 5
	s_cbranch_scc0 .LBB0_879
	s_and_b64 vcc, exec, s[26:27]
	s_cbranch_vccz .LBB0_882
	s_barrier

.LBB0_1126:
	s_add_u32 s81, s46, s50
	s_addc_u32 s82, s47, s51
	s_add_u32 s81, s81, 0x100
	s_addc_u32 s82, s82, 0
	s_and_b64 s[54:55], exec, s[54:55]
	s_cselect_b32 s55, s1, s82
	s_cselect_b32 s54, s37, s81
	s_add_i32 s81, 0, 0x10000
	s_add_i32 s82, 0, 0x14000
	ds_read_b128 v[20:23], v205
	ds_read_b128 v[24:27], v250
	ds_read_b128 v[28:31], v205 offset:2048
	ds_read_b128 v[32:35], v250 offset:2048
	ds_read_b128 v[4:7], v205 offset:16384
	ds_read_b128 v[8:11], v250 offset:16384
	ds_read_b128 v[12:15], v205 offset:18432
	ds_read_b128 v[16:19], v250 offset:18432
	v_lshl_add_u64 v[164:165], v[184:185], 0, s[50:51]
	s_add_i32 m0, s65, 0xc000
	ds_read_b128 v[188:191], v206
	ds_read_b128 v[192:195], v255
	ds_read_b128 v[196:199], v206 offset:2048
	ds_read_b128 v[200:203], v255 offset:2048
	ds_read_b128 v[226:229], v206 offset:4096
	ds_read_b128 v[230:233], v255 offset:4096
	ds_read_b128 v[234:237], v206 offset:6144
	ds_read_b128 v[238:241], v255 offset:6144
	global_load_lds_dwordx4 v[164:165], off
	v_lshl_add_u64 v[164:165], v[186:187], 0, s[50:51]
	s_add_i32 m0, s65, 0xe000
	s_nop 0
	global_load_lds_dwordx4 v[164:165], off
	s_waitcnt vmcnt(8)
	s_waitcnt lgkmcnt(0)
	s_barrier
	s_setprio 1
	v_mfma_f32_16x16x128_f8f6f4 v[160:163], v[20:27], v[188:195], v[160:163]
	v_mfma_f32_16x16x128_f8f6f4 v[156:159], v[28:35], v[188:195], v[156:159]
	v_mfma_f32_16x16x128_f8f6f4 v[144:147], v[20:27], v[196:203], v[144:147]
	v_mfma_f32_16x16x128_f8f6f4 v[140:143], v[28:35], v[196:203], v[140:143]
	v_mfma_f32_16x16x128_f8f6f4 v[128:131], v[20:27], v[226:233], v[128:131]
	v_mfma_f32_16x16x128_f8f6f4 v[124:127], v[28:35], v[226:233], v[124:127]
	v_mfma_f32_16x16x128_f8f6f4 v[112:115], v[20:27], v[234:241], v[112:115]
	v_mfma_f32_16x16x128_f8f6f4 v[108:111], v[28:35], v[234:241], v[108:111]
	v_mfma_f32_16x16x128_f8f6f4 v[152:155], v[4:11], v[188:195], v[152:155]
	v_mfma_f32_16x16x128_f8f6f4 v[148:151], v[12:19], v[188:195], v[148:151]
	v_mfma_f32_16x16x128_f8f6f4 v[136:139], v[4:11], v[196:203], v[136:139]
	v_mfma_f32_16x16x128_f8f6f4 v[132:135], v[12:19], v[196:203], v[132:135]
	v_mfma_f32_16x16x128_f8f6f4 v[120:123], v[4:11], v[226:233], v[120:123]
	v_mfma_f32_16x16x128_f8f6f4 v[116:119], v[12:19], v[226:233], v[116:119]
	v_mfma_f32_16x16x128_f8f6f4 v[104:107], v[4:11], v[234:241], v[104:107]
	v_mfma_f32_16x16x128_f8f6f4 v[100:103], v[12:19], v[234:241], v[100:103]
	s_setprio 0
	s_barrier
	s_add_i32 s81, s81, s62
	v_lshl_add_u64 v[190:191], s[52:53], 0, v[174:175]
	s_mov_b32 m0, s81
	ds_read_b128 v[196:199], v206 offset:16384
	ds_read_b128 v[200:203], v255 offset:16384
	ds_read_b128 v[226:229], v206 offset:18432
	ds_read_b128 v[230:233], v255 offset:18432
	ds_read_b128 v[234:237], v206 offset:20480
	ds_read_b128 v[238:241], v255 offset:20480
	ds_read_b128 v[242:245], v206 offset:22528
	ds_read_b128 v[246:249], v255 offset:22528
	global_load_lds_dwordx4 v[190:191], off
	s_add_i32 m0, s81, 0x2000
	s_add_u32 s84, s52, 0x10000
	v_lshl_add_u64 v[192:193], s[52:53], 0, v[178:179]
	s_addc_u32 s85, s53, 0
	s_add_i32 s81, s82, s62
	global_load_lds_dwordx4 v[192:193], off
	v_lshl_add_u64 v[164:165], s[84:85], 0, v[174:175]
	s_mov_b32 m0, s81
	v_lshl_add_u64 v[194:195], s[54:55], 0, v[172:173]
	global_load_lds_dwordx4 v[164:165], off
	v_lshl_add_u64 v[164:165], s[84:85], 0, v[178:179]
	s_add_i32 m0, s81, 0x2000
	v_lshl_add_u64 v[188:189], s[54:55], 0, v[176:177]
	global_load_lds_dwordx4 v[164:165], off
	s_mov_b32 m0, s65
	s_nop 0
	global_load_lds_dwordx4 v[194:195], off
	s_mov_b32 m0, s66
	s_nop 0
	global_load_lds_dwordx4 v[188:189], off
	s_waitcnt vmcnt(8)
	s_waitcnt lgkmcnt(0)
	s_barrier
	s_setprio 1
	v_mfma_f32_16x16x128_f8f6f4 v[96:99], v[20:27], v[196:203], v[96:99]
	v_mfma_f32_16x16x128_f8f6f4 v[92:95], v[28:35], v[196:203], v[92:95]
	v_mfma_f32_16x16x128_f8f6f4 v[80:83], v[20:27], v[226:233], v[80:83]
	v_mfma_f32_16x16x128_f8f6f4 v[76:79], v[28:35], v[226:233], v[76:79]
	v_mfma_f32_16x16x128_f8f6f4 v[64:67], v[20:27], v[234:241], v[64:67]
	v_mfma_f32_16x16x128_f8f6f4 v[60:63], v[28:35], v[234:241], v[60:63]
	v_mfma_f32_16x16x128_f8f6f4 v[48:51], v[20:27], v[242:249], v[48:51]
	v_mfma_f32_16x16x128_f8f6f4 v[44:47], v[28:35], v[242:249], v[44:47]
	v_mfma_f32_16x16x128_f8f6f4 v[88:91], v[4:11], v[196:203], v[88:91]
	v_mfma_f32_16x16x128_f8f6f4 v[84:87], v[12:19], v[196:203], v[84:87]
	v_mfma_f32_16x16x128_f8f6f4 v[72:75], v[4:11], v[226:233], v[72:75]
	v_mfma_f32_16x16x128_f8f6f4 v[68:71], v[12:19], v[226:233], v[68:71]
	v_mfma_f32_16x16x128_f8f6f4 v[56:59], v[4:11], v[234:241], v[56:59]
	v_mfma_f32_16x16x128_f8f6f4 v[52:55], v[12:19], v[234:241], v[52:55]
	v_mfma_f32_16x16x128_f8f6f4 v[40:43], v[4:11], v[242:249], v[40:43]
	v_mfma_f32_16x16x128_f8f6f4 v[36:39], v[12:19], v[242:249], v[36:39]
	s_setprio 0
	s_barrier
	s_add_i32 s81, 0, 0x18000
	s_add_i32 s82, 0, 0x1c000
	ds_read_b128 v[4:7], v205 offset:32768
	ds_read_b128 v[8:11], v250 offset:32768
	ds_read_b128 v[12:15], v205 offset:34816
	ds_read_b128 v[16:19], v250 offset:34816
	ds_read_b128 v[20:23], v205 offset:49152
	ds_read_b128 v[24:27], v250 offset:49152
	ds_read_b128 v[28:31], v205 offset:51200
	ds_read_b128 v[32:35], v250 offset:51200
	s_add_u32 s54, s54, 0x20000
	s_addc_u32 s55, s55, 0
	s_mov_b32 m0, s67
	v_lshl_add_u64 v[164:165], s[54:55], 0, v[172:173]
	ds_read_b128 v[196:199], v206 offset:32768
	ds_read_b128 v[200:203], v255 offset:32768
	ds_read_b128 v[226:229], v206 offset:34816
	ds_read_b128 v[230:233], v255 offset:34816
	ds_read_b128 v[234:237], v206 offset:36864
	ds_read_b128 v[238:241], v255 offset:36864
	ds_read_b128 v[242:245], v206 offset:38912
	ds_read_b128 v[246:249], v255 offset:38912
	global_load_lds_dwordx4 v[164:165], off
	v_lshl_add_u64 v[164:165], s[54:55], 0, v[176:177]
	s_mov_b32 m0, s68
	s_nop 0
	global_load_lds_dwordx4 v[164:165], off
	s_waitcnt vmcnt(8)
	s_waitcnt lgkmcnt(0)
	s_barrier
	s_setprio 1
	v_mfma_f32_16x16x128_f8f6f4 v[160:163], v[4:11], v[196:203], v[160:163]
	v_mfma_f32_16x16x128_f8f6f4 v[156:159], v[12:19], v[196:203], v[156:159]
	v_mfma_f32_16x16x128_f8f6f4 v[144:147], v[4:11], v[226:233], v[144:147]
	v_mfma_f32_16x16x128_f8f6f4 v[140:143], v[12:19], v[226:233], v[140:143]
	v_mfma_f32_16x16x128_f8f6f4 v[128:131], v[4:11], v[234:241], v[128:131]
	v_mfma_f32_16x16x128_f8f6f4 v[124:127], v[12:19], v[234:241], v[124:127]
	v_mfma_f32_16x16x128_f8f6f4 v[112:115], v[4:11], v[242:249], v[112:115]
	v_mfma_f32_16x16x128_f8f6f4 v[108:111], v[12:19], v[242:249], v[108:111]
	v_mfma_f32_16x16x128_f8f6f4 v[152:155], v[20:27], v[196:203], v[152:155]
	v_mfma_f32_16x16x128_f8f6f4 v[148:151], v[28:35], v[196:203], v[148:151]
	v_mfma_f32_16x16x128_f8f6f4 v[136:139], v[20:27], v[226:233], v[136:139]
	v_mfma_f32_16x16x128_f8f6f4 v[132:135], v[28:35], v[226:233], v[132:135]
	v_mfma_f32_16x16x128_f8f6f4 v[120:123], v[20:27], v[234:241], v[120:123]
	v_mfma_f32_16x16x128_f8f6f4 v[116:119], v[28:35], v[234:241], v[116:119]
	v_mfma_f32_16x16x128_f8f6f4 v[104:107], v[20:27], v[242:249], v[104:107]
	v_mfma_f32_16x16x128_f8f6f4 v[100:103], v[28:35], v[242:249], v[100:103]
	s_setprio 0
	s_barrier
	s_mov_b64 s[84:85], 0x80
	s_add_i32 s54, s81, s62
	v_lshl_add_u64 v[164:165], v[190:191], 0, s[84:85]
	s_mov_b32 m0, s54
	ds_read_b128 v[196:199], v206 offset:49152
	ds_read_b128 v[200:203], v255 offset:49152
	ds_read_b128 v[226:229], v206 offset:51200
	ds_read_b128 v[230:233], v255 offset:51200
	ds_read_b128 v[234:237], v206 offset:53248
	ds_read_b128 v[238:241], v255 offset:53248
	ds_read_b128 v[242:245], v206 offset:55296
	ds_read_b128 v[246:249], v255 offset:55296
	global_load_lds_dwordx4 v[164:165], off
	s_add_i32 m0, s54, 0x2000
	s_add_u32 s52, s52, 0x10080
	v_lshl_add_u64 v[164:165], v[192:193], 0, s[84:85]
	s_addc_u32 s53, s53, 0
	s_add_i32 s54, s82, s62
	global_load_lds_dwordx4 v[164:165], off
	v_lshl_add_u64 v[164:165], s[52:53], 0, v[174:175]
	s_mov_b32 m0, s54
	s_nop 0
	global_load_lds_dwordx4 v[164:165], off
	v_lshl_add_u64 v[164:165], s[52:53], 0, v[178:179]
	s_add_i32 m0, s54, 0x2000
	s_nop 0
	global_load_lds_dwordx4 v[164:165], off
	v_lshl_add_u64 v[164:165], v[194:195], 0, s[84:85]
	s_mov_b32 m0, s71
	s_nop 0
	global_load_lds_dwordx4 v[164:165], off
	v_lshl_add_u64 v[164:165], v[188:189], 0, s[84:85]
	s_mov_b32 m0, s72
	s_nop 0
	global_load_lds_dwordx4 v[164:165], off
	s_waitcnt vmcnt(8)
	s_waitcnt lgkmcnt(0)
	s_barrier
	s_setprio 1
	v_mfma_f32_16x16x128_f8f6f4 v[96:99], v[4:11], v[196:203], v[96:99]
	v_mfma_f32_16x16x128_f8f6f4 v[92:95], v[12:19], v[196:203], v[92:95]
	v_mfma_f32_16x16x128_f8f6f4 v[80:83], v[4:11], v[226:233], v[80:83]
	v_mfma_f32_16x16x128_f8f6f4 v[76:79], v[12:19], v[226:233], v[76:79]
	v_mfma_f32_16x16x128_f8f6f4 v[64:67], v[4:11], v[234:241], v[64:67]
	v_mfma_f32_16x16x128_f8f6f4 v[60:63], v[12:19], v[234:241], v[60:63]
	v_mfma_f32_16x16x128_f8f6f4 v[48:51], v[4:11], v[242:249], v[48:51]
	v_mfma_f32_16x16x128_f8f6f4 v[44:47], v[12:19], v[242:249], v[44:47]
	v_mfma_f32_16x16x128_f8f6f4 v[88:91], v[20:27], v[196:203], v[88:91]
	v_mfma_f32_16x16x128_f8f6f4 v[84:87], v[28:35], v[196:203], v[84:87]
	v_mfma_f32_16x16x128_f8f6f4 v[72:75], v[20:27], v[226:233], v[72:75]
	v_mfma_f32_16x16x128_f8f6f4 v[68:71], v[28:35], v[226:233], v[68:71]
	v_mfma_f32_16x16x128_f8f6f4 v[56:59], v[20:27], v[234:241], v[56:59]
	v_mfma_f32_16x16x128_f8f6f4 v[52:55], v[28:35], v[234:241], v[52:55]
	v_mfma_f32_16x16x128_f8f6f4 v[40:43], v[20:27], v[242:249], v[40:43]
	v_mfma_f32_16x16x128_f8f6f4 v[36:39], v[28:35], v[242:249], v[36:39]
	s_setprio 0
	s_barrier
	s_add_u32 s50, s50, 0x100
	s_mov_b64 s[52:53], s[88:89]
	s_addc_u32 s51, s51, 0
	s_add_i32 s52, s52, 2
	s_cmp_gt_u32 s52, 5
	s_cbranch_scc1 .LBB0_1129
